# attn_fast: the join before A^T waits only for the LDS tiles (vmcnt(8)); the 8 gate-row loads are waited right before the epilogue
# speedup vs baseline: 1.0453x; 1.0083x over previous
.Lat_join:
	s_waitcnt vmcnt(8)
	s_barrier
	s_cmp_lt_u32 s44, 0x100
	s_cbranch_scc1 .Lat_cont
	ds_read_b128 v[70:73], v152
	ds_read_b128 v[76:79], v152 offset:1024
	ds_read_b64 v[0:1], v153 offset:2048
	ds_read_b64 v[10:11], v153 offset:2560
	ds_read_b64 v[14:15], v153 offset:3072
	ds_read_b64 v[18:19], v153 offset:3584
	ds_read_b64 v[40:41], v153 offset:4096
	ds_read_b64 v[80:81], v153 offset:4608
	ds_read_b32 v20, v154 offset:5120
	s_waitcnt lgkmcnt(0)
.Lat_cont:
	ds_read2st64_b64 v[26:29], v17 offset1:4
	ds_read2st64_b64 v[30:33], v58 offset1:4
	v_rcp_f32_e32 v34, v70
	v_rcp_f32_e32 v35, v71
	v_add_u32_e32 v67, v16, v107
	v_add_u32_e32 v74, v16, v108
	v_pk_mul_f32 v[0:1], v[0:1], v[40:41] op_sel_hi:[0,1]
	ds_read2st64_b64 v[38:41], v67 offset1:4
	ds_read2st64_b64 v[42:45], v74 offset1:4
	v_pk_mul_f32 v[84:85], v[0:1], v[34:35]
	s_waitcnt lgkmcnt(0)
	v_mov_b32_e32 v34, v26
	v_mov_b32_e32 v35, v27
	v_mov_b32_e32 v36, v30
	v_mov_b32_e32 v37, v31
	v_mov_b32_e32 v30, v28
	v_mov_b32_e32 v31, v29
	v_cvt_pk_bf16_f32 v21, v72, v73
	v_mov_b32_e32 v68, v38
	v_mov_b32_e32 v69, v39
	v_mov_b32_e32 v70, v42
	v_mov_b32_e32 v71, v43
	v_mov_b32_e32 v42, v40
	v_mov_b32_e32 v43, v41
	v_mfma_f32_16x16x32_bf16 v[34:37], v[34:37], v[18:21], 0
	v_cvt_pk_bf16_f32 v22, v76, v77
	v_cvt_pk_bf16_f32 v23, v78, v79
	v_cvt_pk_bf16_f32 v24, v80, v81
	v_mfma_f32_16x16x32_bf16 v[30:33], v[30:33], v[18:21], 0
	v_cvt_pk_bf16_f32 v25, v84, v85
	v_cvt_pk_f16_f32 v16, v10, v11
	v_pk_mul_f32 v[0:1], v[12:13], v[72:73]
	v_mfma_f32_16x16x32_bf16 v[26:29], v[68:71], v[22:25], v[34:37]
	ds_read2st64_b64 v[68:71], v74 offset0:8 offset1:12
	v_pk_mul_f32 v[2:3], v[2:3], v[80:81]
	v_pk_mul_f32 v[4:5], v[4:5], v[84:85]
	ds_read2st64_b64 v[34:37], v17 offset0:8 offset1:12
	v_mfma_f32_16x16x32_bf16 v[10:13], v[42:45], v[22:25], v[30:33]
	ds_read2st64_b64 v[42:45], v67 offset0:8 offset1:12
	s_waitcnt lgkmcnt(0)
	v_mov_b32_e32 v74, v68
	v_mov_b32_e32 v75, v69
	ds_read2st64_b64 v[30:33], v58 offset0:8 offset1:12
	v_mov_b32_e32 v38, v34
	v_mov_b32_e32 v39, v35
	v_mov_b32_e32 v72, v42
	v_mov_b32_e32 v73, v43
	s_waitcnt lgkmcnt(0)
	v_mov_b32_e32 v40, v30
	v_mov_b32_e32 v41, v31
	v_mov_b32_e32 v30, v36
	v_mov_b32_e32 v31, v37
	v_mfma_f32_16x16x32_bf16 v[38:41], v[38:41], v[18:21], 0
	v_mov_b32_e32 v68, v44
	v_mov_b32_e32 v69, v45
	v_cvt_pk_f16_f32 v17, v0, v1
	v_pk_mul_f32 v[0:1], v[6:7], v[76:77]
	v_mfma_f32_16x16x32_bf16 v[34:37], v[72:75], v[22:25], v[38:41]
	v_cvt_f16_f32_e32 v10, v10
	v_cvt_f16_f32_e32 v11, v11
	v_cvt_f16_f32_e32 v12, v12
	v_pk_mul_f32 v[38:39], v[8:9], v[78:79]
	v_mfma_f32_16x16x32_bf16 v[6:9], v[30:33], v[18:21], 0
	v_cvt_f16_f32_e32 v13, v13
	v_cvt_f16_f32_e32 v20, v28
	v_cvt_f16_f32_e32 v21, v29
	v_mfma_f32_16x16x32_bf16 v[6:9], v[68:71], v[22:25], v[6:9]
	v_cndmask_b32_e64 v10, v10, 0, s[8:9]
	v_cndmask_b32_e64 v11, v11, 0, s[10:11]
	v_cvt_f16_f32_e32 v18, v26
	v_cvt_f16_f32_e32 v19, v27
	v_cndmask_b32_e64 v12, v12, 0, s[16:17]
	v_cndmask_b32_e64 v13, v13, 0, s[20:21]
	v_pack_b32_f16 v44, v10, v11
	v_cvt_f16_f32_e32 v10, v34
	v_cvt_f16_f32_e32 v11, v35
	v_cndmask_b32_e64 v20, v20, 0, s[4:5]
	v_cndmask_b32_e64 v21, v21, 0, s[6:7]
	v_pack_b32_f16 v45, v12, v13
	v_cvt_f16_f32_e32 v12, v36
	v_cvt_f16_f32_e32 v13, v37
	v_cvt_f16_f32_e32 v6, v6
	v_cvt_f16_f32_e32 v7, v7
	v_cvt_f16_f32_e32 v8, v8
	v_cvt_f16_f32_e32 v9, v9
	v_pack_b32_f16 v43, v20, v21
	v_lshl_or_b32 v20, v66, 14, v112
	v_add3_u32 v36, s3, v111, v20
	v_cndmask_b32_e64 v18, v18, 0, vcc
	v_cndmask_b32_e64 v19, 0, v19, s[0:1]
	v_cndmask_b32_e64 v10, v10, 0, s[12:13]
	v_cndmask_b32_e64 v11, v11, 0, s[14:15]
	v_add_u32_e32 v58, v36, v109
	v_add_u32_e32 v67, v36, v110
	v_cvt_pk_f16_f32 v0, v0, v1
	v_cvt_pk_f16_f32 v1, v38, v39
	v_pack_b32_f16 v42, v18, v19
	v_cndmask_b32_e64 v18, v12, 0, s[18:19]
	v_cndmask_b32_e64 v19, v13, 0, s[22:23]
	v_cndmask_b32_e64 v30, v6, 0, s[24:25]
	v_cndmask_b32_e64 v31, v7, 0, s[26:27]
	v_cndmask_b32_e64 v34, v8, 0, s[28:29]
	v_cndmask_b32_e64 v35, v9, 0, s[30:31]
	v_pack_b32_f16 v38, v10, v11
	ds_read2st64_b64 v[6:9], v58 offset1:4
	ds_read2st64_b64 v[10:13], v67 offset1:4
	v_add3_u32 v37, s33, v111, v20
	v_add_u32_e32 v96, v37, v109
	v_add_u32_e32 v97, v37, v110
	ds_read2st64_b64 v[22:25], v96 offset1:4
	ds_read2st64_b64 v[26:29], v97 offset1:4
	v_pack_b32_f16 v39, v18, v19
	s_waitcnt lgkmcnt(0)
	v_mov_b32_e32 v18, v6
	v_mov_b32_e32 v19, v7
	v_mov_b32_e32 v20, v10
	v_mov_b32_e32 v21, v11
	v_add_u32_e32 v98, v36, v107
	v_add_u32_e32 v99, v36, v108
	v_pack_b32_f16 v40, v30, v31
	v_mov_b32_e32 v30, v22
	v_mov_b32_e32 v31, v23
	v_mov_b32_e32 v32, v26
	v_mov_b32_e32 v33, v27
	ds_read2st64_b64 v[68:71], v98 offset1:4
	ds_read2st64_b64 v[72:75], v99 offset1:4
	v_mfma_f32_16x16x32_f16 v[18:21], v[18:21], v[42:45], 0
	v_mov_b32_e32 v10, v8
	v_mov_b32_e32 v11, v9
	v_add_u32_e32 v100, v37, v107
	v_add_u32_e32 v101, v37, v108
	ds_read2st64_b64 v[76:79], v100 offset1:4
	ds_read2st64_b64 v[80:83], v101 offset1:4
	v_mfma_f32_16x16x32_f16 v[18:21], v[30:33], v[14:17], v[18:21]
	s_waitcnt lgkmcnt(0)
	v_mov_b32_e32 v30, v68
	v_mov_b32_e32 v31, v69
	v_mov_b32_e32 v32, v72
	v_mov_b32_e32 v33, v73
	v_mov_b32_e32 v26, v24
	v_mov_b32_e32 v27, v25
	v_cvt_pk_f16_f32 v2, v2, v3
	v_cvt_pk_f16_f32 v3, v4, v5
	v_mfma_f32_16x16x32_f16 v[4:7], v[10:13], v[42:45], 0
	v_pack_b32_f16 v41, v34, v35
	v_mov_b32_e32 v34, v76
	v_mov_b32_e32 v35, v77
	v_mov_b32_e32 v36, v80
	v_mov_b32_e32 v37, v81
	v_mfma_f32_16x16x32_f16 v[18:21], v[30:33], v[38:41], v[18:21]
	v_mov_b32_e32 v72, v70
	v_mov_b32_e32 v73, v71
	v_mov_b32_e32 v80, v78
	v_mfma_f32_16x16x32_f16 v[4:7], v[26:29], v[14:17], v[4:7]
	v_mov_b32_e32 v81, v79
	s_mov_b32 s1, 0
	v_cmp_eq_u32_e32 vcc, 0, v104
	v_mfma_f32_16x16x32_f16 v[34:37], v[34:37], v[0:3], v[18:21]
	ds_read2st64_b64 v[8:11], v58 offset0:8 offset1:12
	s_nop 1
	ds_read2st64_b64 v[18:21], v67 offset0:8 offset1:12
	ds_read2st64_b64 v[22:25], v96 offset0:8 offset1:12
	ds_read2st64_b64 v[68:71], v97 offset0:8 offset1:12
	s_nop 1
	v_mul_f32_e32 v12, v35, v35
	v_mfma_f32_16x16x32_f16 v[4:7], v[72:75], v[38:41], v[4:7]
	s_waitcnt lgkmcnt(0)
	v_mov_b32_e32 v26, v22
	v_mov_b32_e32 v27, v23
	v_mov_b32_e32 v28, v68
	v_mfma_f32_16x16x32_f16 v[30:33], v[80:83], v[0:3], v[4:7]
	v_mov_b32_e32 v29, v69
	ds_read2st64_b64 v[72:75], v98 offset0:8 offset1:12
	ds_read2st64_b64 v[76:79], v99 offset0:8 offset1:12
	v_mov_b32_e32 v4, v8
	v_mov_b32_e32 v5, v9
	v_mov_b32_e32 v6, v18
	v_mov_b32_e32 v7, v19
	ds_read2st64_b64 v[80:83], v100 offset0:8 offset1:12
	ds_read2st64_b64 v[84:87], v101 offset0:8 offset1:12
	v_mfma_f32_16x16x32_f16 v[4:7], v[4:7], v[42:45], 0
	v_mov_b32_e32 v18, v10
	v_mov_b32_e32 v19, v11
	v_mov_b32_e32 v68, v24
	v_mfma_f32_16x16x32_f16 v[4:7], v[26:29], v[14:17], v[4:7]
	s_waitcnt lgkmcnt(0)
	v_mov_b32_e32 v26, v72
	v_mov_b32_e32 v27, v73
	v_mov_b32_e32 v28, v76
	v_mov_b32_e32 v29, v77
	v_mov_b32_e32 v69, v25
	v_mov_b32_e32 v76, v74
	v_mfma_f32_16x16x32_f16 v[4:7], v[26:29], v[38:41], v[4:7]
	v_mov_b32_e32 v26, v80
	v_mov_b32_e32 v27, v81
	v_mov_b32_e32 v28, v84
	v_mov_b32_e32 v29, v85
	v_mov_b32_e32 v77, v75
	v_mov_b32_e32 v84, v82
	v_mfma_f32_16x16x32_f16 v[26:29], v[26:29], v[0:3], v[4:7]
	v_mov_b32_e32 v85, v83
	v_mul_f32_e32 v13, v31, v31
	v_fmac_f32_e32 v12, v34, v34
	v_mfma_f32_16x16x32_f16 v[4:7], v[18:21], v[42:45], 0
	v_fmac_f32_e32 v13, v30, v30
	v_fmac_f32_e32 v12, v36, v36
	v_fmac_f32_e32 v13, v32, v32
	v_mfma_f32_16x16x32_f16 v[4:7], v[68:71], v[14:17], v[4:7]
	ds_read2st64_b64 v[8:11], v58 offset0:16 offset1:20
	ds_read2st64_b64 v[68:71], v67 offset0:16 offset1:20
	v_fmac_f32_e32 v12, v37, v37
	v_fmac_f32_e32 v13, v33, v33
	v_mfma_f32_16x16x32_f16 v[4:7], v[76:79], v[38:41], v[4:7]
	ds_read2st64_b64 v[72:75], v96 offset0:16 offset1:20
	ds_read2st64_b64 v[76:79], v97 offset0:16 offset1:20
	v_add_f32_e32 v12, v12, v13
	v_mul_f32_e32 v13, v27, v27
	v_mfma_f32_16x16x32_f16 v[22:25], v[84:87], v[0:3], v[4:7]
	s_waitcnt lgkmcnt(0)
	v_mov_b32_e32 v18, v72
	v_mov_b32_e32 v19, v73
	v_mov_b32_e32 v20, v76
	v_mov_b32_e32 v4, v8
	v_mov_b32_e32 v5, v9
	v_mov_b32_e32 v6, v68
	v_mov_b32_e32 v7, v69
	v_mov_b32_e32 v21, v77
	ds_read2st64_b64 v[80:83], v98 offset0:16 offset1:20
	ds_read2st64_b64 v[84:87], v99 offset0:16 offset1:20
	v_mfma_f32_16x16x32_f16 v[4:7], v[4:7], v[42:45], 0
	ds_read2st64_b64 v[88:91], v100 offset0:16 offset1:20
	ds_read2st64_b64 v[92:95], v101 offset0:16 offset1:20
	v_mov_b32_e32 v68, v10
	v_mov_b32_e32 v69, v11
	v_mfma_f32_16x16x32_f16 v[4:7], v[18:21], v[14:17], v[4:7]
	s_waitcnt lgkmcnt(0)
	v_mov_b32_e32 v18, v80
	v_mov_b32_e32 v19, v81
	v_mov_b32_e32 v20, v84
	v_mov_b32_e32 v21, v85
	v_mov_b32_e32 v76, v74
	v_mov_b32_e32 v77, v75
	v_mfma_f32_16x16x32_f16 v[4:7], v[18:21], v[38:41], v[4:7]
	v_mov_b32_e32 v18, v88
	v_mov_b32_e32 v19, v89
	v_mov_b32_e32 v20, v92
	v_mov_b32_e32 v21, v93
	v_mov_b32_e32 v84, v82
	v_mov_b32_e32 v85, v83
	v_mfma_f32_16x16x32_f16 v[18:21], v[18:21], v[0:3], v[4:7]
	v_mov_b32_e32 v92, v90
	v_mov_b32_e32 v93, v91
	v_fmac_f32_e32 v13, v26, v26
	v_mfma_f32_16x16x32_f16 v[4:7], v[68:71], v[42:45], 0
	ds_read2st64_b64 v[68:71], v58 offset0:24 offset1:28
	ds_read2st64_b64 v[72:75], v67 offset0:24 offset1:28
	v_fmac_f32_e32 v13, v28, v28
	v_fmac_f32_e32 v13, v29, v29
	v_mfma_f32_16x16x32_f16 v[4:7], v[76:79], v[14:17], v[4:7]
	ds_read2st64_b64 v[76:79], v96 offset0:24 offset1:28
	ds_read2st64_b64 v[80:83], v97 offset0:24 offset1:28
	v_add_f32_e32 v12, v12, v13
	v_mul_f32_e32 v13, v23, v23
	v_mfma_f32_16x16x32_f16 v[4:7], v[84:87], v[38:41], v[4:7]
	v_fmac_f32_e32 v13, v22, v22
	v_fmac_f32_e32 v13, v24, v24
	v_fmac_f32_e32 v13, v25, v25
	v_mfma_f32_16x16x32_f16 v[8:11], v[92:95], v[0:3], v[4:7]
	s_waitcnt lgkmcnt(0)
	v_mov_b32_e32 v84, v76
	v_mov_b32_e32 v85, v77
	v_mov_b32_e32 v86, v80
	v_mov_b32_e32 v4, v68
	v_mov_b32_e32 v5, v69
	v_mov_b32_e32 v6, v72
	v_mov_b32_e32 v7, v73
	v_mov_b32_e32 v72, v70
	v_mov_b32_e32 v73, v71
	v_mov_b32_e32 v87, v81
	ds_read2st64_b64 v[88:91], v98 offset0:24 offset1:28
	ds_read2st64_b64 v[92:95], v99 offset0:24 offset1:28
	v_add_f32_e32 v12, v12, v13
	v_mul_f32_e32 v13, v19, v19
	v_mfma_f32_16x16x32_f16 v[4:7], v[4:7], v[42:45], 0
	v_fmac_f32_e32 v13, v18, v18
	v_fmac_f32_e32 v13, v20, v20
	v_mov_b32_e32 v80, v78
	v_mov_b32_e32 v81, v79
	v_fmac_f32_e32 v13, v21, v21
	v_mfma_f32_16x16x32_f16 v[42:45], v[72:75], v[42:45], 0
	v_add_f32_e32 v12, v12, v13
	v_mul_f32_e32 v13, v9, v9
	ds_read2st64_b64 v[96:99], v100 offset0:24 offset1:28
	ds_read2st64_b64 v[108:111], v101 offset0:24 offset1:28
	v_mfma_f32_16x16x32_f16 v[4:7], v[84:87], v[14:17], v[4:7]
	s_waitcnt lgkmcnt(0)
	v_mov_b32_e32 v84, v88
	v_mov_b32_e32 v85, v89
	v_mov_b32_e32 v86, v92
	v_mov_b32_e32 v87, v93
	v_fmac_f32_e32 v13, v8, v8
	v_fmac_f32_e32 v13, v10, v10
	v_fmac_f32_e32 v13, v11, v11
	v_mov_b32_e32 v92, v90
	v_mov_b32_e32 v93, v91
	v_add_f32_e32 v58, v12, v13
	v_mfma_f32_16x16x32_f16 v[12:15], v[80:83], v[14:17], v[42:45]
	v_mfma_f32_16x16x32_f16 v[4:7], v[84:87], v[38:41], v[4:7]
	v_mov_b32_e32 v84, v96
	v_mov_b32_e32 v85, v97
	v_mov_b32_e32 v86, v108
	v_mov_b32_e32 v87, v109
	v_mov_b32_e32 v108, v98
	v_mov_b32_e32 v109, v99
	v_mfma_f32_16x16x32_f16 v[12:15], v[92:95], v[38:41], v[12:15]
	v_mfma_f32_16x16x32_f16 v[4:7], v[84:87], v[0:3], v[4:7]
	v_mfma_f32_16x16x32_f16 v[0:3], v[108:111], v[0:3], v[12:15]
	s_nop 5
	v_and_b32_e32 v14, 0x70, v105
	v_mul_f32_e32 v67, v5, v5
	v_fmac_f32_e32 v67, v4, v4
	v_mul_f32_e32 v12, v1, v1
	v_fmac_f32_e32 v67, v6, v6
	v_fmac_f32_e32 v12, v0, v0
	v_fmac_f32_e32 v67, v7, v7
	v_fmac_f32_e32 v12, v2, v2
	v_add_f32_e32 v16, v58, v67
	v_fmac_f32_e32 v12, v3, v3
	v_add_f32_e32 v12, v16, v12
	ds_bpermute_b32 v13, v64, v12
	s_waitcnt lgkmcnt(0)
	v_add_f32_e32 v12, v12, v13
	ds_bpermute_b32 v15, v65, v12
	v_lshlrev_b32_e32 v13, 7, v66
	s_waitcnt lgkmcnt(0)
	v_add_f32_e32 v12, v12, v15
	s_and_saveexec_b64 s[4:5], vcc
	v_lshlrev_b32_e32 v15, 2, v14
	s_add_i32 s0, 0, 0x26600
	v_lshlrev_b32_e32 v16, 2, v103
	v_add3_u32 v15, s0, v15, v16
	ds_write_b32 v15, v12
	s_or_b64 exec, exec, s[4:5]
	v_bitop3_b32 v14, v14, 64, v103 bitop3:0x36
	v_lshl_add_u32 v14, v14, 2, 0
	v_add_u32_e32 v14, 0x26600, v14
	s_waitcnt vmcnt(0) lgkmcnt(0)
	s_barrier
	s_waitcnt vmcnt(0)
	ds_read_b32 v38, v14
	v_cvt_f32_f16_e32 v40, v62
	s_mov_b32 s4, 0x800000
	v_or_b32_e32 v13, v13, v106
	v_lshl_add_u32 v14, v13, 2, 0
	s_waitcnt lgkmcnt(0)
	v_add_f32_e32 v12, v12, v38
	v_mov_b32_e32 v38, 0x3727c5ac
	v_fmac_f32_e32 v38, 0x33800000, v12
	v_mul_f32_e32 v12, 0x4b800000, v38
	v_cmp_gt_f32_e32 vcc, s4, v38
	v_mul_f32_e32 v41, 0xbfb8aa3b, v40
	v_exp_f32_e32 v42, v41
	v_cndmask_b32_e32 v12, v38, v12, vcc
	v_cvt_f32_f16_sdwa v41, v62 dst_sel:DWORD dst_unused:UNUSED_PAD src0_sel:WORD_1
	v_rsq_f32_e32 v12, v12
	v_add_u32_e32 v44, 0x26200, v14
	ds_read_b128 v[14:17], v44
	v_mul_f32_e32 v43, 0xbfb8aa3b, v41
	v_mul_f32_e32 v38, 0x45800000, v12
	v_exp_f32_e32 v43, v43
	v_cndmask_b32_e32 v12, v12, v38, vcc
	v_mul_f32_e32 v12, 0x3b800000, v12
	v_pk_mul_f32 v[34:35], v[12:13], v[34:35] op_sel_hi:[0,1]
	s_waitcnt lgkmcnt(0)
	v_pk_mul_f32 v[14:15], v[14:15], v[34:35]
	v_add_f32_e32 v34, 1.0, v43
	v_rcp_f32_e32 v43, v34
	v_cvt_f32_f16_e32 v34, v63
	v_add_f32_e32 v42, 1.0, v42
	v_cvt_f32_f16_sdwa v35, v63 dst_sel:DWORD dst_unused:UNUSED_PAD src0_sel:WORD_1
	v_rcp_f32_e32 v42, v42
	v_pk_mul_f32 v[14:15], v[14:15], v[40:41]
	v_mul_f32_e32 v40, 0xbfb8aa3b, v34
	v_exp_f32_e32 v41, v40
	v_mul_f32_e32 v40, 0xbfb8aa3b, v35
	v_pk_mul_f32 v[14:15], v[14:15], v[42:43]
	v_exp_f32_e32 v42, v40
	v_cvt_pk_f16_f32 v40, v14, v15
	v_add_f32_e32 v14, 1.0, v41
	v_rcp_f32_e32 v14, v14
	v_add_f32_e32 v15, 1.0, v42
	v_rcp_f32_e32 v15, v15
	s_lshl_b32 s0, s2, 4
	s_lshl_b32 s2, s2, 6
	v_pk_mul_f32 v[36:37], v[12:13], v[36:37] op_sel_hi:[0,1]
	s_and_b32 s3, s0, 0xfffff800
	s_and_b32 s2, s2, 0x7c0
	v_pk_mul_f32 v[16:17], v[16:17], v[36:37]
	s_or_b32 s2, s3, s2
	v_pk_mul_f32 v[16:17], v[16:17], v[34:35]
	v_or_b32_e32 v38, s2, v102
	v_pk_mul_f32 v[14:15], v[16:17], v[14:15]
	v_cvt_f32_f16_e32 v16, v60
	v_ashrrev_i32_e32 v39, 31, v38
	v_cvt_f32_f16_sdwa v17, v60 dst_sel:DWORD dst_unused:UNUSED_PAD src0_sel:WORD_1
	v_lshlrev_b64 v[38:39], 11, v[38:39]
	v_lshl_add_u64 v[38:39], s[42:43], 0, v[38:39]
	s_and_b32 s0, s0, 0x600
	v_lshl_add_u64 v[38:39], v[38:39], 0, s[0:1]
	v_lshlrev_b32_e32 v58, 1, v13
	v_mul_f32_e32 v13, 0xbfb8aa3b, v16
	v_cvt_pk_f16_f32 v41, v14, v15
	v_lshl_add_u64 v[14:15], v[38:39], 0, v[58:59]
	v_exp_f32_e32 v13, v13
	v_mul_f32_e32 v38, 0xbfb8aa3b, v17
	ds_read_b128 v[34:37], v44 offset:64
	v_exp_f32_e32 v38, v38
	v_add_f32_e32 v13, 1.0, v13
	v_rcp_f32_e32 v42, v13
	v_pk_mul_f32 v[30:31], v[12:13], v[30:31] op_sel_hi:[0,1]
	v_add_f32_e32 v13, 1.0, v38
	global_store_dwordx2 v[14:15], v[40:41], off
	v_rcp_f32_e32 v43, v13
	ds_read_b128 v[38:41], v44 offset:128
	s_waitcnt lgkmcnt(1)
	v_pk_mul_f32 v[30:31], v[34:35], v[30:31]
	v_cvt_f32_f16_e32 v34, v61
	v_cvt_f32_f16_sdwa v35, v61 dst_sel:DWORD dst_unused:UNUSED_PAD src0_sel:WORD_1
	v_pk_mul_f32 v[16:17], v[30:31], v[16:17]
	v_mul_f32_e32 v13, 0xbfb8aa3b, v34
	v_pk_mul_f32 v[16:17], v[16:17], v[42:43]
	v_exp_f32_e32 v13, v13
	v_cvt_pk_f16_f32 v16, v16, v17
	v_mul_f32_e32 v17, 0xbfb8aa3b, v35
	v_exp_f32_e32 v17, v17
	v_add_f32_e32 v13, 1.0, v13
	v_rcp_f32_e32 v30, v13
	v_pk_mul_f32 v[32:33], v[12:13], v[32:33] op_sel_hi:[0,1]
	v_add_f32_e32 v13, 1.0, v17
	v_rcp_f32_e32 v31, v13
	v_cvt_f32_f16_e32 v42, v56
	v_pk_mul_f32 v[32:33], v[36:37], v[32:33]
	v_cvt_f32_f16_sdwa v43, v56 dst_sel:DWORD dst_unused:UNUSED_PAD src0_sel:WORD_1
	v_pk_mul_f32 v[32:33], v[32:33], v[34:35]
	v_mul_f32_e32 v13, 0xbfb8aa3b, v42
	v_pk_mul_f32 v[30:31], v[32:33], v[30:31]
	v_exp_f32_e32 v13, v13
	v_cvt_pk_f16_f32 v17, v30, v31
	global_store_dwordx2 v[14:15], v[16:17], off offset:32
	v_mul_f32_e32 v16, 0xbfb8aa3b, v43
	v_exp_f32_e32 v17, v16
	v_add_f32_e32 v13, 1.0, v13
	v_rcp_f32_e32 v16, v13
	v_pk_mul_f32 v[26:27], v[12:13], v[26:27] op_sel_hi:[0,1]
	v_add_f32_e32 v13, 1.0, v17
	v_cvt_f32_f16_e32 v30, v57
	v_rcp_f32_e32 v17, v13
	v_cvt_f32_f16_sdwa v31, v57 dst_sel:DWORD dst_unused:UNUSED_PAD src0_sel:WORD_1
	s_waitcnt lgkmcnt(0)
	v_pk_mul_f32 v[26:27], v[38:39], v[26:27]
	v_mul_f32_e32 v13, 0xbfb8aa3b, v30
	v_pk_mul_f32 v[26:27], v[26:27], v[42:43]
	v_exp_f32_e32 v13, v13
	v_pk_mul_f32 v[16:17], v[26:27], v[16:17]
	v_mul_f32_e32 v26, 0xbfb8aa3b, v31
	v_exp_f32_e32 v27, v26
	v_add_f32_e32 v13, 1.0, v13
	v_rcp_f32_e32 v26, v13
	v_cvt_f32_f16_e32 v34, v52
	v_add_f32_e32 v13, 1.0, v27
	v_rcp_f32_e32 v27, v13
	v_pk_mul_f32 v[28:29], v[12:13], v[28:29] op_sel_hi:[0,1]
	v_pk_mul_f32 v[28:29], v[40:41], v[28:29]
	v_cvt_f32_f16_sdwa v35, v52 dst_sel:DWORD dst_unused:UNUSED_PAD src0_sel:WORD_1
	v_pk_mul_f32 v[28:29], v[28:29], v[30:31]
	v_cvt_pk_f16_f32 v16, v16, v17
	v_pk_mul_f32 v[26:27], v[28:29], v[26:27]
	v_mul_f32_e32 v13, 0xbfb8aa3b, v34
	v_cvt_pk_f16_f32 v17, v26, v27
	global_store_dwordx2 v[14:15], v[16:17], off offset:64
	v_exp_f32_e32 v13, v13
	v_mul_f32_e32 v16, 0xbfb8aa3b, v35
	ds_read_b128 v[26:29], v44 offset:192
	ds_read_b128 v[30:33], v44 offset:256
	v_exp_f32_e32 v17, v16
	v_add_f32_e32 v13, 1.0, v13
	v_rcp_f32_e32 v16, v13
	v_pk_mul_f32 v[22:23], v[12:13], v[22:23] op_sel_hi:[0,1]
	v_add_f32_e32 v13, 1.0, v17
	v_rcp_f32_e32 v17, v13
	s_waitcnt lgkmcnt(1)
	v_pk_mul_f32 v[22:23], v[26:27], v[22:23]
	v_cvt_f32_f16_e32 v26, v53
	v_cvt_f32_f16_sdwa v27, v53 dst_sel:DWORD dst_unused:UNUSED_PAD src0_sel:WORD_1
	v_pk_mul_f32 v[22:23], v[22:23], v[34:35]
	v_cvt_f32_f16_e32 v34, v54
	v_pk_mul_f32 v[16:17], v[22:23], v[16:17]
	v_mul_f32_e32 v13, 0xbfb8aa3b, v26
	v_exp_f32_e32 v13, v13
	v_cvt_pk_f16_f32 v16, v16, v17
	v_mul_f32_e32 v17, 0xbfb8aa3b, v27
	v_exp_f32_e32 v17, v17
	v_add_f32_e32 v13, 1.0, v13
	v_rcp_f32_e32 v22, v13
	v_pk_mul_f32 v[24:25], v[12:13], v[24:25] op_sel_hi:[0,1]
	v_add_f32_e32 v13, 1.0, v17
	v_rcp_f32_e32 v23, v13
	v_pk_mul_f32 v[24:25], v[28:29], v[24:25]
	v_cvt_f32_f16_sdwa v35, v54 dst_sel:DWORD dst_unused:UNUSED_PAD src0_sel:WORD_1
	v_pk_mul_f32 v[24:25], v[24:25], v[26:27]
	v_mul_f32_e32 v13, 0xbfb8aa3b, v34
	v_pk_mul_f32 v[22:23], v[24:25], v[22:23]
	v_exp_f32_e32 v13, v13
	v_cvt_pk_f16_f32 v17, v22, v23
	global_store_dwordx2 v[14:15], v[16:17], off offset:96
	v_mul_f32_e32 v16, 0xbfb8aa3b, v35
	v_exp_f32_e32 v17, v16
	v_add_f32_e32 v13, 1.0, v13
	v_rcp_f32_e32 v16, v13
	v_pk_mul_f32 v[18:19], v[12:13], v[18:19] op_sel_hi:[0,1]
	v_add_f32_e32 v13, 1.0, v17
	v_cvt_f32_f16_e32 v22, v55
	v_rcp_f32_e32 v17, v13
	v_cvt_f32_f16_sdwa v23, v55 dst_sel:DWORD dst_unused:UNUSED_PAD src0_sel:WORD_1
	s_waitcnt lgkmcnt(0)
	v_pk_mul_f32 v[18:19], v[30:31], v[18:19]
	v_mul_f32_e32 v13, 0xbfb8aa3b, v22
	v_pk_mul_f32 v[18:19], v[18:19], v[34:35]
	v_exp_f32_e32 v13, v13
	v_pk_mul_f32 v[16:17], v[18:19], v[16:17]
	v_mul_f32_e32 v18, 0xbfb8aa3b, v23
	v_exp_f32_e32 v19, v18
	v_add_f32_e32 v13, 1.0, v13
	v_rcp_f32_e32 v18, v13
	v_cvt_f32_f16_e32 v24, v50
	v_add_f32_e32 v13, 1.0, v19
	v_rcp_f32_e32 v19, v13
	v_cvt_f32_f16_sdwa v25, v50 dst_sel:DWORD dst_unused:UNUSED_PAD src0_sel:WORD_1
	v_pk_mul_f32 v[20:21], v[12:13], v[20:21] op_sel_hi:[0,1]
	v_pk_mul_f32 v[20:21], v[32:33], v[20:21]
	v_mul_f32_e32 v13, 0xbfb8aa3b, v24
	v_pk_mul_f32 v[20:21], v[20:21], v[22:23]
	v_exp_f32_e32 v13, v13
	v_pk_mul_f32 v[18:19], v[20:21], v[18:19]
	v_mul_f32_e32 v20, 0xbfb8aa3b, v25
	v_cvt_pk_f16_f32 v16, v16, v17
	v_cvt_pk_f16_f32 v17, v18, v19
	v_exp_f32_e32 v20, v20
	global_store_dwordx2 v[14:15], v[16:17], off offset:128
	ds_read_b128 v[16:19], v44 offset:320
	v_add_f32_e32 v13, 1.0, v13
	v_rcp_f32_e32 v26, v13
	v_pk_mul_f32 v[8:9], v[12:13], v[8:9] op_sel_hi:[0,1]
	v_add_f32_e32 v13, 1.0, v20
	v_rcp_f32_e32 v27, v13
	ds_read_b128 v[20:23], v44 offset:384
	s_waitcnt lgkmcnt(1)
	v_pk_mul_f32 v[8:9], v[16:17], v[8:9]
	v_cvt_f32_f16_e32 v16, v51
	v_cvt_f32_f16_sdwa v17, v51 dst_sel:DWORD dst_unused:UNUSED_PAD src0_sel:WORD_1
	v_pk_mul_f32 v[8:9], v[8:9], v[24:25]
	v_mul_f32_e32 v13, 0xbfb8aa3b, v16
	v_pk_mul_f32 v[8:9], v[8:9], v[26:27]
	v_exp_f32_e32 v13, v13
	v_cvt_pk_f16_f32 v8, v8, v9
	v_mul_f32_e32 v9, 0xbfb8aa3b, v17
	v_exp_f32_e32 v9, v9
	v_add_f32_e32 v13, 1.0, v13
	v_rcp_f32_e32 v24, v13
	v_pk_mul_f32 v[10:11], v[12:13], v[10:11] op_sel_hi:[0,1]
	v_add_f32_e32 v9, 1.0, v9
	v_rcp_f32_e32 v25, v9
	v_pk_mul_f32 v[10:11], v[18:19], v[10:11]
	v_pk_mul_f32 v[4:5], v[12:13], v[4:5] op_sel_hi:[0,1]
	v_pk_mul_f32 v[10:11], v[10:11], v[16:17]
	v_cvt_f32_f16_e32 v16, v48
	v_cvt_f32_f16_sdwa v17, v48 dst_sel:DWORD dst_unused:UNUSED_PAD src0_sel:WORD_1
	v_pk_mul_f32 v[10:11], v[10:11], v[24:25]
	s_waitcnt lgkmcnt(0)
	v_pk_mul_f32 v[4:5], v[20:21], v[4:5]
	v_cvt_pk_f16_f32 v9, v10, v11
	v_mul_f32_e32 v10, 0xbfb8aa3b, v16
	global_store_dwordx2 v[14:15], v[8:9], off offset:160
	v_mul_f32_e32 v8, 0xbfb8aa3b, v17
	v_exp_f32_e32 v10, v10
	v_exp_f32_e32 v9, v8
	v_cvt_f32_f16_sdwa v11, v49 dst_sel:DWORD dst_unused:UNUSED_PAD src0_sel:WORD_1
	v_pk_mul_f32 v[4:5], v[4:5], v[16:17]
	v_add_f32_e32 v8, 1.0, v10
	v_add_f32_e32 v9, 1.0, v9
	v_rcp_f32_e32 v8, v8
	v_rcp_f32_e32 v9, v9
	v_cvt_f32_f16_e32 v10, v49
	v_pk_mul_f32 v[6:7], v[12:13], v[6:7] op_sel_hi:[0,1]
	v_cvt_f32_f16_e32 v16, v46
	v_pk_mul_f32 v[4:5], v[4:5], v[8:9]
	v_mul_f32_e32 v8, 0xbfb8aa3b, v10
	v_cvt_pk_f16_f32 v4, v4, v5
	v_mul_f32_e32 v5, 0xbfb8aa3b, v11
	v_exp_f32_e32 v8, v8
	v_exp_f32_e32 v5, v5
	v_pk_mul_f32 v[6:7], v[22:23], v[6:7]
	v_cvt_f32_f16_sdwa v17, v46 dst_sel:DWORD dst_unused:UNUSED_PAD src0_sel:WORD_1
	v_add_f32_e32 v8, 1.0, v8
	v_add_f32_e32 v5, 1.0, v5
	v_rcp_f32_e32 v8, v8
	v_rcp_f32_e32 v9, v5
	v_pk_mul_f32 v[6:7], v[6:7], v[10:11]
	v_pk_mul_f32 v[0:1], v[12:13], v[0:1] op_sel_hi:[0,1]
	v_pk_mul_f32 v[2:3], v[12:13], v[2:3] op_sel_hi:[0,1]
	v_pk_mul_f32 v[6:7], v[6:7], v[8:9]
	v_mul_f32_e32 v9, 0xbfb8aa3b, v17
	v_cvt_pk_f16_f32 v5, v6, v7
	v_mul_f32_e32 v6, 0xbfb8aa3b, v16
	v_exp_f32_e32 v8, v6
	global_store_dwordx2 v[14:15], v[4:5], off offset:192
	ds_read_b128 v[4:7], v44 offset:448
	v_exp_f32_e32 v9, v9
	v_add_f32_e32 v8, 1.0, v8
	v_rcp_f32_e32 v8, v8
	s_waitcnt lgkmcnt(0)
	v_pk_mul_f32 v[0:1], v[4:5], v[0:1]
	v_add_f32_e32 v4, 1.0, v9
	v_rcp_f32_e32 v9, v4
	v_cvt_f32_f16_e32 v4, v47
	v_cvt_f32_f16_sdwa v5, v47 dst_sel:DWORD dst_unused:UNUSED_PAD src0_sel:WORD_1
	v_pk_mul_f32 v[0:1], v[0:1], v[16:17]
	v_pk_mul_f32 v[2:3], v[6:7], v[2:3]
	v_pk_mul_f32 v[0:1], v[0:1], v[8:9]
	v_mul_f32_e32 v8, 0xbfb8aa3b, v4
	v_exp_f32_e32 v8, v8
	v_mul_f32_e32 v9, 0xbfb8aa3b, v5
	v_exp_f32_e32 v9, v9
	v_cvt_pk_f16_f32 v0, v0, v1
	v_add_f32_e32 v1, 1.0, v8
	v_rcp_f32_e32 v8, v1
	v_add_f32_e32 v1, 1.0, v9
	v_rcp_f32_e32 v9, v1
	v_pk_mul_f32 v[2:3], v[2:3], v[4:5]
	s_nop 0
	v_pk_mul_f32 v[2:3], v[2:3], v[8:9]
	s_nop 0
	v_cvt_pk_f16_f32 v1, v2, v3
	global_store_dwordx2 v[14:15], v[0:1], off offset:224
	s_endpgm
